# v50 plus stagger step 0 (GEMM phases start all workgroups at once)
# speedup vs baseline: 1.0225x; 1.0062x over previous
; __global__ void __launch_bounds__(NWAVES * 64, 2) fwd_kernel(Args a_unused) {
;     ...
;         { const unsigned long long t0_ = __builtin_amdgcn_s_memrealtime(); const unsigned long long dl_ = (unsigned long long)(vcu & 7) * (STAG_TICKS / 2);
;           while (__builtin_amdgcn_s_memrealtime() - t0_ < dl_) __builtin_amdgcn_s_sleep(4); }
.LBB0_446:
	s_and_b64 vcc, exec, s[4:5]
	s_cbranch_vccz .LBB0_1126
	s_memrealtime s[4:5]
	s_waitcnt lgkmcnt(0)
	s_memrealtime s[8:9]
	s_and_b32 s3, s97, 7
	s_mov_b32 s7, 0
	s_mul_i32 s6, s3, 0
	s_waitcnt vmcnt(11)
	v_mov_b64_e32 v[2:3], s[6:7]
	s_waitcnt lgkmcnt(0)
	s_sub_u32 s8, s8, s4
	s_subb_u32 s9, s9, s5
	v_cmp_ge_u64_e32 vcc, s[8:9], v[2:3]
	s_mov_b32 s50, s95
	s_cbranch_vccnz .LBB0_450
	v_mov_b64_e32 v[2:3], s[6:7]

; __global__ void __launch_bounds__(NWAVES * 64, 2) fwd_kernel(Args a_unused) {
;     ...
;         { const unsigned long long t0_ = __builtin_amdgcn_s_memrealtime(); const unsigned long long dl_ = (unsigned long long)(vcu & 7) * (STAG_TICKS / 2);
;           while (__builtin_amdgcn_s_memrealtime() - t0_ < dl_) __builtin_amdgcn_s_sleep(4); }
.LBB0_1453:
	s_cmp_lt_i32 s46, 7
	s_cselect_b64 s[6:7], -1, 0
	s_and_b64 s[6:7], s[6:7], s[4:5]
	s_andn2_b64 vcc, exec, s[6:7]
	s_cbranch_vccnz .LBB0_1501
	s_mov_b64 s[4:5], s[0:1]
	s_waitcnt lgkmcnt(0)
	s_load_dwordx2 s[8:9], s[4:5], 0xc8
	s_and_b32 s3, s97, 7
	s_memrealtime s[4:5]
	s_memrealtime s[12:13]
	s_mul_i32 s10, s3, 0
	s_mov_b32 s11, 0
	s_waitcnt vmcnt(0)
	v_mov_b64_e32 v[2:3], s[10:11]
	s_waitcnt lgkmcnt(0)
	s_sub_u32 s12, s12, s4
	s_subb_u32 s13, s13, s5
	v_cmp_ge_u64_e32 vcc, s[12:13], v[2:3]
	s_cbranch_vccnz .LBB0_1457
	v_mov_b64_e32 v[2:3], s[10:11]

; __global__ void __launch_bounds__(NWAVES * 64, 2) fwd_kernel(Args a_unused) {
;     ...
;         { const unsigned long long t0_ = __builtin_amdgcn_s_memrealtime(); const unsigned long long dl_ = (unsigned long long)(vcu & 7) * (STAG_TICKS / 2);
;           while (__builtin_amdgcn_s_memrealtime() - t0_ < dl_) __builtin_amdgcn_s_sleep(4); }
.LBB0_1615:
	s_or_b64 exec, exec, s[4:5]
	s_waitcnt lgkmcnt(0)
	s_barrier
	s_load_dwordx2 s[10:11], s[10:11], 0x0
	s_and_b32 s3, s97, 7
	s_memrealtime s[4:5]
	s_memrealtime s[14:15]
	s_mul_i32 s12, s3, 0
	s_mov_b32 s13, 0
	v_mov_b64_e32 v[2:3], s[12:13]
	s_waitcnt lgkmcnt(0)
	s_sub_u32 s14, s14, s4
	s_subb_u32 s15, s15, s5
	v_cmp_ge_u64_e32 vcc, s[14:15], v[2:3]
	s_cbranch_vccnz .LBB0_1618
	v_mov_b64_e32 v[2:3], s[12:13]

; __global__ void __launch_bounds__(NWAVES * 64, 2) fwd_kernel(Args a_unused) {
;     ...
;         { const unsigned long long t0_ = __builtin_amdgcn_s_memrealtime(); const unsigned long long dl_ = (unsigned long long)(vcu & 7) * (STAG_TICKS / 2);
;           while (__builtin_amdgcn_s_memrealtime() - t0_ < dl_) __builtin_amdgcn_s_sleep(4); }
.LBB0_2249:
	s_or_b64 exec, exec, s[4:5]
	s_waitcnt lgkmcnt(0)
	s_barrier
	s_load_dwordx2 s[4:5], s[8:9], 0x90
	s_load_dwordx2 s[6:7], s[8:9], 0xa0
	s_and_b32 s3, s97, 7
	s_memrealtime s[8:9]
	s_memrealtime s[16:17]
	s_mul_i32 s14, s3, 0
	s_mov_b32 s15, 0
	v_mov_b64_e32 v[2:3], s[14:15]
	s_waitcnt lgkmcnt(0)
	s_sub_u32 s16, s16, s8
	s_subb_u32 s17, s17, s9
	v_cmp_ge_u64_e32 vcc, s[16:17], v[2:3]
	s_cbranch_vccnz .LBB0_2252
	v_mov_b64_e32 v[2:3], s[14:15]

; __global__ void __launch_bounds__(NWAVES * 64, 2) fwd_kernel(Args a_unused) {
;     ...
;         { const unsigned long long t0_ = __builtin_amdgcn_s_memrealtime(); const unsigned long long dl_ = (unsigned long long)(vcu & 7) * (STAG_TICKS / 2);
;           while (__builtin_amdgcn_s_memrealtime() - t0_ < dl_) __builtin_amdgcn_s_sleep(4); }
.LBB0_2420:
	s_or_b64 exec, exec, s[4:5]
	s_waitcnt lgkmcnt(0)
	s_barrier
	s_load_dwordx2 s[14:15], s[6:7], 0xb0
	s_memrealtime s[4:5]
	s_memrealtime s[8:9]
	s_and_b32 s3, s97, 7
	s_mul_i32 s6, s3, 0
	s_mov_b32 s7, 0
	v_mov_b64_e32 v[2:3], s[6:7]
	s_waitcnt lgkmcnt(0)
	s_sub_u32 s8, s8, s4
	s_subb_u32 s9, s9, s5
	v_cmp_ge_u64_e32 vcc, s[8:9], v[2:3]
	s_cbranch_vccnz .LBB0_2423
	v_mov_b64_e32 v[2:3], s[6:7]
